# same without the weight-conversion load batching (adaLN batching kept)
# speedup vs baseline: 1.0237x; 1.0053x over previous
.LBB0_19:
	v_lshl_add_u64 v[54:55], v[32:33], 0, s[6:7]
	v_lshl_add_u64 v[56:57], v[30:31], 0, s[6:7]
	v_lshl_add_u64 v[58:59], v[28:29], 0, s[6:7]
	v_lshl_add_u64 v[60:61], v[26:27], 0, s[6:7]
	v_lshl_add_u64 v[62:63], v[24:25], 0, s[6:7]
	v_lshl_add_u64 v[64:65], v[22:23], 0, s[6:7]
	v_lshl_add_u64 v[66:67], v[20:21], 0, s[6:7]
	v_lshl_add_u64 v[68:69], v[18:19], 0, s[6:7]
	global_load_dword v53, v[54:55], off nt
	global_load_dword v70, v[56:57], off nt
	global_load_dword v71, v[58:59], off nt
	global_load_dword v72, v[60:61], off nt
	global_load_dword v73, v[62:63], off nt
	global_load_dword v74, v[64:65], off nt
	global_load_dword v75, v[66:67], off nt
	global_load_dword v76, v[68:69], off nt
	s_add_u32 s6, s6, 0x10000
	s_addc_u32 s7, s7, 0
	v_add_u32_e32 v54, 0x400, v52
	s_cmp_lg_u32 s6, 0x40000
	s_waitcnt vmcnt(7)
	v_mul_f32_e32 v53, 0x42800000, v53
	s_waitcnt vmcnt(6)
	v_mul_f32_e32 v55, 0x42800000, v70
	s_waitcnt vmcnt(5)
	v_mul_f32_e32 v56, 0x42800000, v71
	s_waitcnt vmcnt(4)
	v_mul_f32_e32 v57, 0x42800000, v72
	s_waitcnt vmcnt(3)
	v_mul_f32_e32 v58, 0x42800000, v73
	s_waitcnt vmcnt(2)
	v_mul_f32_e32 v59, 0x42800000, v74
	s_waitcnt vmcnt(1)
	v_mul_f32_e32 v60, 0x42800000, v75
	s_waitcnt vmcnt(0)
	v_mul_f32_e32 v61, 0x42800000, v76
	ds_write2_b32 v52, v53, v55 offset1:66
	ds_write2_b32 v52, v56, v57 offset0:132 offset1:198
	ds_write2_b32 v54, v58, v59 offset0:8 offset1:74
	ds_write2_b32 v54, v60, v61 offset0:140 offset1:206
	v_add_u32_e32 v52, 0x840, v52
	s_cbranch_scc1 .LBB0_19
	s_waitcnt lgkmcnt(0)
	ds_read2_b32 v[22:23], v37 offset0:66 offset1:99
	ds_read2_b32 v[18:19], v37 offset1:33
	v_mov_b32_e32 v24, 0x43e00000
	s_add_i32 s2, s17, 0xfffde000
	s_waitcnt lgkmcnt(1)
	v_med3_f32 v26, v22, -v24, v24
	v_med3_f32 v27, v23, -v24, v24
	ds_read2_b32 v[22:23], v37 offset0:132 offset1:165
	s_waitcnt lgkmcnt(1)
	v_med3_f32 v25, v18, -v24, v24
	v_med3_f32 v19, v19, -v24, v24
	v_mov_b32_e32 v18, v3
	v_cvt_pk_fp8_f32 v18, v25, v19
	ds_read2_b32 v[24:25], v37 offset0:198 offset1:231
	v_mov_b32_e32 v28, 0x43e00000
	s_lshr_b32 s2, s2, 9
	v_mov_b32_e32 v19, v3
	s_waitcnt lgkmcnt(1)
	v_med3_f32 v22, v22, -v28, v28
	v_med3_f32 v23, v23, -v28, v28
	s_lshl_b64 s[6:7], s[2:3], 20
	s_lshl_b32 s2, s17, 1
	s_lshl_b32 s12, s17, 5
	v_cvt_pk_fp8_f32 v19, v22, v23
	s_and_b32 s2, s2, 0x3c0
	s_and_b32 s12, s12, 0x3e0
	s_add_u32 s6, s19, s6
	s_addc_u32 s7, s20, s7
	s_waitcnt lgkmcnt(0)
	v_med3_f32 v22, v24, -v28, v28
	v_med3_f32 v23, v25, -v28, v28
	s_add_u32 s6, s6, s2
	v_cvt_pk_fp8_f32 v18, v26, v27 op_sel:[0,0,1]
	v_cvt_pk_fp8_f32 v19, v22, v23 op_sel:[0,0,1]
	s_addc_u32 s7, s7, 0
	v_or_b32_e32 v22, s12, v36
	v_lshl_add_u64 v[20:21], s[6:7], 0, v[0:1]
	v_lshlrev_b32_e32 v22, 10, v22
	v_mov_b32_e32 v23, v3
	v_lshl_add_u64 v[22:23], v[20:21], 0, v[22:23]
	ds_read2_b32 v[24:25], v37 offset0:8 offset1:41
	global_store_dwordx2 v[22:23], v[18:19], off
	ds_read2_b32 v[18:19], v37 offset0:74 offset1:107
	v_mov_b32_e32 v22, 0x43e00000
	v_mov_b32_e32 v28, 0x43e00000
	s_waitcnt lgkmcnt(1)
	v_med3_f32 v24, v24, -v22, v22
	v_med3_f32 v25, v25, -v22, v22
	s_waitcnt lgkmcnt(0)
	v_med3_f32 v26, v18, -v22, v22
	v_med3_f32 v27, v19, -v22, v22
	ds_read2_b32 v[22:23], v37 offset0:140 offset1:173
	v_mov_b32_e32 v18, v3
	v_cvt_pk_fp8_f32 v18, v24, v25
	ds_read2_b32 v[24:25], v37 offset0:206 offset1:239
	v_mov_b32_e32 v19, v3
	s_waitcnt lgkmcnt(1)
	v_med3_f32 v22, v22, -v28, v28
	v_med3_f32 v23, v23, -v28, v28
	v_cvt_pk_fp8_f32 v19, v22, v23
	s_waitcnt lgkmcnt(0)
	v_med3_f32 v22, v24, -v28, v28
	v_med3_f32 v23, v25, -v28, v28
	v_cvt_pk_fp8_f32 v18, v26, v27 op_sel:[0,0,1]
	v_cvt_pk_fp8_f32 v19, v22, v23 op_sel:[0,0,1]
	v_or_b32_e32 v22, s12, v38
	v_lshlrev_b32_e32 v22, 10, v22
	v_mov_b32_e32 v23, v3
	v_lshl_add_u64 v[22:23], v[20:21], 0, v[22:23]
	ds_read2_b32 v[24:25], v37 offset0:16 offset1:49
	global_store_dwordx2 v[22:23], v[18:19], off
	ds_read2_b32 v[18:19], v37 offset0:82 offset1:115
	v_mov_b32_e32 v22, 0x43e00000
	v_mov_b32_e32 v28, 0x43e00000
	s_waitcnt lgkmcnt(1)
	v_med3_f32 v24, v24, -v22, v22
	v_med3_f32 v25, v25, -v22, v22
	s_waitcnt lgkmcnt(0)
	v_med3_f32 v26, v18, -v22, v22
	v_med3_f32 v27, v19, -v22, v22
	ds_read2_b32 v[22:23], v37 offset0:148 offset1:181
	v_mov_b32_e32 v18, v3
	v_cvt_pk_fp8_f32 v18, v24, v25
	ds_read2_b32 v[24:25], v37 offset0:214 offset1:247
	v_mov_b32_e32 v19, v3
	s_waitcnt lgkmcnt(1)
	v_med3_f32 v22, v22, -v28, v28
	v_med3_f32 v23, v23, -v28, v28
	v_cvt_pk_fp8_f32 v19, v22, v23
	s_waitcnt lgkmcnt(0)
	v_med3_f32 v22, v24, -v28, v28
	v_med3_f32 v23, v25, -v28, v28
	v_cvt_pk_fp8_f32 v18, v26, v27 op_sel:[0,0,1]
	v_cvt_pk_fp8_f32 v19, v22, v23 op_sel:[0,0,1]
	v_or_b32_e32 v22, s12, v39
	v_lshlrev_b32_e32 v22, 10, v22
	v_mov_b32_e32 v23, v3
	v_lshl_add_u64 v[22:23], v[20:21], 0, v[22:23]
	ds_read2_b32 v[24:25], v37 offset0:24 offset1:57
	global_store_dwordx2 v[22:23], v[18:19], off
	ds_read2_b32 v[18:19], v37 offset0:90 offset1:123
	v_mov_b32_e32 v22, 0x43e00000
	v_mov_b32_e32 v28, 0x43e00000
	s_waitcnt lgkmcnt(1)
	v_med3_f32 v24, v24, -v22, v22
	v_med3_f32 v25, v25, -v22, v22
	s_waitcnt lgkmcnt(0)
	v_med3_f32 v26, v18, -v22, v22
	v_med3_f32 v27, v19, -v22, v22
	ds_read2_b32 v[22:23], v37 offset0:156 offset1:189
	v_mov_b32_e32 v18, v3
	v_cvt_pk_fp8_f32 v18, v24, v25
	ds_read2_b32 v[24:25], v37 offset0:222 offset1:255
	v_mov_b32_e32 v19, v3
	s_waitcnt lgkmcnt(1)
	v_med3_f32 v22, v22, -v28, v28
	v_med3_f32 v23, v23, -v28, v28
	v_cvt_pk_fp8_f32 v19, v22, v23
	s_waitcnt lgkmcnt(0)
	v_med3_f32 v22, v24, -v28, v28
	v_med3_f32 v23, v25, -v28, v28
	v_cvt_pk_fp8_f32 v18, v26, v27 op_sel:[0,0,1]
	v_cvt_pk_fp8_f32 v19, v22, v23 op_sel:[0,0,1]
	v_or_b32_e32 v22, s12, v40
	v_lshlrev_b32_e32 v22, 10, v22
	v_mov_b32_e32 v23, v3
	v_lshl_add_u64 v[20:21], v[20:21], 0, v[22:23]
	global_store_dwordx2 v[20:21], v[18:19], off
	s_waitcnt lgkmcnt(0)
	s_mov_b64 s[6:7], 0

.LBB0_23:
	v_lshl_add_u64 v[54:55], v[32:33], 0, s[6:7]
	v_lshl_add_u64 v[56:57], v[30:31], 0, s[6:7]
	v_lshl_add_u64 v[58:59], v[28:29], 0, s[6:7]
	v_lshl_add_u64 v[60:61], v[26:27], 0, s[6:7]
	v_lshl_add_u64 v[62:63], v[24:25], 0, s[6:7]
	v_lshl_add_u64 v[64:65], v[22:23], 0, s[6:7]
	v_lshl_add_u64 v[66:67], v[20:21], 0, s[6:7]
	v_lshl_add_u64 v[68:69], v[18:19], 0, s[6:7]
	global_load_dword v53, v[54:55], off nt
	global_load_dword v70, v[56:57], off nt
	global_load_dword v71, v[58:59], off nt
	global_load_dword v72, v[60:61], off nt
	global_load_dword v73, v[62:63], off nt
	global_load_dword v74, v[64:65], off nt
	global_load_dword v75, v[66:67], off nt
	global_load_dword v76, v[68:69], off nt
	s_add_u32 s6, s6, 0x20000
	s_addc_u32 s7, s7, 0
	v_add_u32_e32 v54, 0x400, v52
	s_cmp_lg_u32 s6, 0x80000
	s_waitcnt vmcnt(7)
	v_mul_f32_e32 v53, 0x42800000, v53
	s_waitcnt vmcnt(6)
	v_mul_f32_e32 v55, 0x42800000, v70
	s_waitcnt vmcnt(5)
	v_mul_f32_e32 v56, 0x42800000, v71
	s_waitcnt vmcnt(4)
	v_mul_f32_e32 v57, 0x42800000, v72
	s_waitcnt vmcnt(3)
	v_mul_f32_e32 v58, 0x42800000, v73
	s_waitcnt vmcnt(2)
	v_mul_f32_e32 v59, 0x42800000, v74
	s_waitcnt vmcnt(1)
	v_mul_f32_e32 v60, 0x42800000, v75
	s_waitcnt vmcnt(0)
	v_mul_f32_e32 v61, 0x42800000, v76
	ds_write2_b32 v52, v53, v55 offset1:66
	ds_write2_b32 v52, v56, v57 offset0:132 offset1:198
	ds_write2_b32 v54, v58, v59 offset0:8 offset1:74
	ds_write2_b32 v54, v60, v61 offset0:140 offset1:206
	v_add_u32_e32 v52, 0x840, v52
	s_cbranch_scc1 .LBB0_23
	s_waitcnt lgkmcnt(0)
	ds_read2_b32 v[22:23], v37 offset0:66 offset1:99
	ds_read2_b32 v[18:19], v37 offset1:33
	v_mov_b32_e32 v24, 0x43e00000
	s_add_i32 s2, s17, 0xffffe000
	s_waitcnt lgkmcnt(1)
	v_med3_f32 v26, v22, -v24, v24
	v_med3_f32 v27, v23, -v24, v24
	ds_read2_b32 v[22:23], v37 offset0:132 offset1:165
	s_waitcnt lgkmcnt(1)
	v_med3_f32 v25, v18, -v24, v24
	v_med3_f32 v19, v19, -v24, v24
	v_mov_b32_e32 v18, v3
	v_cvt_pk_fp8_f32 v18, v25, v19
	ds_read2_b32 v[24:25], v37 offset0:198 offset1:231
	v_mov_b32_e32 v28, 0x43e00000
	s_lshr_b32 s2, s2, 10
	v_mov_b32_e32 v19, v3
	s_waitcnt lgkmcnt(1)
	v_med3_f32 v22, v22, -v28, v28
	v_med3_f32 v23, v23, -v28, v28
	s_lshl_b64 s[6:7], s[2:3], 21
	v_cvt_pk_fp8_f32 v19, v22, v23
	s_add_u32 s2, s21, s6
	s_addc_u32 s7, s22, s7
	s_lshl_b32 s6, s17, 5
	s_and_b32 s13, s6, 0x7e0
	s_waitcnt lgkmcnt(0)
	v_med3_f32 v22, v24, -v28, v28
	v_med3_f32 v23, v25, -v28, v28
	s_add_u32 s6, s2, s12
	v_cvt_pk_fp8_f32 v18, v26, v27 op_sel:[0,0,1]
	v_cvt_pk_fp8_f32 v19, v22, v23 op_sel:[0,0,1]
	s_addc_u32 s7, s7, 0
	v_or_b32_e32 v22, s13, v36
	v_lshl_add_u64 v[20:21], s[6:7], 0, v[0:1]
	v_lshlrev_b32_e32 v22, 10, v22
	v_mov_b32_e32 v23, v3
	v_lshl_add_u64 v[22:23], v[20:21], 0, v[22:23]
	ds_read2_b32 v[24:25], v37 offset0:8 offset1:41
	global_store_dwordx2 v[22:23], v[18:19], off
	ds_read2_b32 v[18:19], v37 offset0:74 offset1:107
	v_mov_b32_e32 v22, 0x43e00000
	v_mov_b32_e32 v28, 0x43e00000
	s_waitcnt lgkmcnt(1)
	v_med3_f32 v24, v24, -v22, v22
	v_med3_f32 v25, v25, -v22, v22
	s_waitcnt lgkmcnt(0)
	v_med3_f32 v26, v18, -v22, v22
	v_med3_f32 v27, v19, -v22, v22
	ds_read2_b32 v[22:23], v37 offset0:140 offset1:173
	v_mov_b32_e32 v18, v3
	v_cvt_pk_fp8_f32 v18, v24, v25
	ds_read2_b32 v[24:25], v37 offset0:206 offset1:239
	v_mov_b32_e32 v19, v3
	s_waitcnt lgkmcnt(1)
	v_med3_f32 v22, v22, -v28, v28
	v_med3_f32 v23, v23, -v28, v28
	v_cvt_pk_fp8_f32 v19, v22, v23
	s_waitcnt lgkmcnt(0)
	v_med3_f32 v22, v24, -v28, v28
	v_med3_f32 v23, v25, -v28, v28
	v_cvt_pk_fp8_f32 v18, v26, v27 op_sel:[0,0,1]
	v_cvt_pk_fp8_f32 v19, v22, v23 op_sel:[0,0,1]
	v_or_b32_e32 v22, s13, v38
	v_lshlrev_b32_e32 v22, 10, v22
	v_mov_b32_e32 v23, v3
	v_lshl_add_u64 v[22:23], v[20:21], 0, v[22:23]
	ds_read2_b32 v[24:25], v37 offset0:16 offset1:49
	global_store_dwordx2 v[22:23], v[18:19], off
	ds_read2_b32 v[18:19], v37 offset0:82 offset1:115
	v_mov_b32_e32 v22, 0x43e00000
	v_mov_b32_e32 v28, 0x43e00000
	s_waitcnt lgkmcnt(1)
	v_med3_f32 v24, v24, -v22, v22
	v_med3_f32 v25, v25, -v22, v22
	s_waitcnt lgkmcnt(0)
	v_med3_f32 v26, v18, -v22, v22
	v_med3_f32 v27, v19, -v22, v22
	ds_read2_b32 v[22:23], v37 offset0:148 offset1:181
	v_mov_b32_e32 v18, v3
	v_cvt_pk_fp8_f32 v18, v24, v25
	ds_read2_b32 v[24:25], v37 offset0:214 offset1:247
	v_mov_b32_e32 v19, v3
	s_waitcnt lgkmcnt(1)
	v_med3_f32 v22, v22, -v28, v28
	v_med3_f32 v23, v23, -v28, v28
	v_cvt_pk_fp8_f32 v19, v22, v23
	s_waitcnt lgkmcnt(0)
	v_med3_f32 v22, v24, -v28, v28
	v_med3_f32 v23, v25, -v28, v28
	v_cvt_pk_fp8_f32 v18, v26, v27 op_sel:[0,0,1]
	v_cvt_pk_fp8_f32 v19, v22, v23 op_sel:[0,0,1]
	v_or_b32_e32 v22, s13, v39
	v_lshlrev_b32_e32 v22, 10, v22
	v_mov_b32_e32 v23, v3
	v_lshl_add_u64 v[22:23], v[20:21], 0, v[22:23]
	ds_read2_b32 v[24:25], v37 offset0:24 offset1:57
	global_store_dwordx2 v[22:23], v[18:19], off
	ds_read2_b32 v[18:19], v37 offset0:90 offset1:123
	v_mov_b32_e32 v22, 0x43e00000
	v_mov_b32_e32 v28, 0x43e00000
	s_waitcnt lgkmcnt(1)
	v_med3_f32 v24, v24, -v22, v22
	v_med3_f32 v25, v25, -v22, v22
	s_waitcnt lgkmcnt(0)
	v_med3_f32 v26, v18, -v22, v22
	v_med3_f32 v27, v19, -v22, v22
	ds_read2_b32 v[22:23], v37 offset0:156 offset1:189
	v_mov_b32_e32 v18, v3
	v_cvt_pk_fp8_f32 v18, v24, v25
	ds_read2_b32 v[24:25], v37 offset0:222 offset1:255
	v_mov_b32_e32 v19, v3
	s_waitcnt lgkmcnt(1)
	v_med3_f32 v22, v22, -v28, v28
	v_med3_f32 v23, v23, -v28, v28
	v_cvt_pk_fp8_f32 v19, v22, v23
	s_waitcnt lgkmcnt(0)
	v_med3_f32 v22, v24, -v28, v28
	v_med3_f32 v23, v25, -v28, v28
	v_cvt_pk_fp8_f32 v18, v26, v27 op_sel:[0,0,1]
	v_cvt_pk_fp8_f32 v19, v22, v23 op_sel:[0,0,1]
	v_or_b32_e32 v22, s13, v40
	v_lshlrev_b32_e32 v22, 10, v22
	v_mov_b32_e32 v23, v3
	v_lshl_add_u64 v[20:21], v[20:21], 0, v[22:23]
	global_store_dwordx2 v[20:21], v[18:19], off
	s_waitcnt lgkmcnt(0)

.LBB0_28:
	v_lshl_add_u64 v[20:21], v[18:19], 0, s[6:7]
	v_lshl_add_u64 v[22:23], v[16:17], 0, s[6:7]
	v_lshl_add_u64 v[24:25], v[14:15], 0, s[6:7]
	v_lshl_add_u64 v[26:27], v[12:13], 0, s[6:7]
	v_lshl_add_u64 v[28:29], v[10:11], 0, s[6:7]
	v_lshl_add_u64 v[30:31], v[8:9], 0, s[6:7]
	v_lshl_add_u64 v[32:33], v[6:7], 0, s[6:7]
	v_lshl_add_u64 v[52:53], v[4:5], 0, s[6:7]
	global_load_dword v51, v[20:21], off nt
	global_load_dword v54, v[22:23], off nt
	global_load_dword v55, v[24:25], off nt
	global_load_dword v56, v[26:27], off nt
	global_load_dword v57, v[28:29], off nt
	global_load_dword v58, v[30:31], off nt
	global_load_dword v59, v[32:33], off nt
	global_load_dword v60, v[52:53], off nt
	s_add_u32 s6, s6, 0x10000
	s_addc_u32 s7, s7, 0
	v_add_u32_e32 v20, 0x400, v2
	s_cmp_lg_u32 s6, 0x40000
	s_waitcnt vmcnt(7)
	v_mul_f32_e32 v21, 0x42800000, v51
	s_waitcnt vmcnt(6)
	v_mul_f32_e32 v22, 0x42800000, v54
	s_waitcnt vmcnt(5)
	v_mul_f32_e32 v23, 0x42800000, v55
	s_waitcnt vmcnt(4)
	v_mul_f32_e32 v24, 0x42800000, v56
	s_waitcnt vmcnt(3)
	v_mul_f32_e32 v25, 0x42800000, v57
	s_waitcnt vmcnt(2)
	v_mul_f32_e32 v26, 0x42800000, v58
	s_waitcnt vmcnt(1)
	v_mul_f32_e32 v27, 0x42800000, v59
	s_waitcnt vmcnt(0)
	v_mul_f32_e32 v28, 0x42800000, v60
	ds_write2_b32 v2, v21, v22 offset1:66
	ds_write2_b32 v2, v23, v24 offset0:132 offset1:198
	ds_write2_b32 v20, v25, v26 offset0:8 offset1:74
	ds_write2_b32 v20, v27, v28 offset0:140 offset1:206
	v_add_u32_e32 v2, 0x840, v2
	s_cbranch_scc1 .LBB0_28
	s_waitcnt lgkmcnt(0)
	ds_read2_b32 v[4:5], v37 offset1:33
	ds_read2_b32 v[8:9], v37 offset0:66 offset1:99
	v_mov_b32_e32 v2, 0x43e00000
	s_add_i32 s2, s17, 0xffffe800
	s_waitcnt lgkmcnt(1)
	v_med3_f32 v10, v4, -v2, v2
	v_med3_f32 v5, v5, -v2, v2
	s_waitcnt lgkmcnt(0)
	v_med3_f32 v12, v8, -v2, v2
	v_med3_f32 v2, v9, -v2, v2
	ds_read2_b32 v[8:9], v37 offset0:132 offset1:165
	v_mov_b32_e32 v4, v3
	v_cvt_pk_fp8_f32 v4, v10, v5
	ds_read2_b32 v[10:11], v37 offset0:198 offset1:231
	v_mov_b32_e32 v13, 0x43e00000
	s_lshr_b32 s2, s2, 9
	v_mov_b32_e32 v5, v3
	s_waitcnt lgkmcnt(1)
	v_med3_f32 v8, v8, -v13, v13
	v_med3_f32 v9, v9, -v13, v13
	s_lshl_b64 s[6:7], s[2:3], 20
	s_lshl_b32 s2, s17, 1
	s_lshl_b32 s12, s17, 5
	v_cvt_pk_fp8_f32 v5, v8, v9
	s_and_b32 s2, s2, 0x3c0
	s_and_b32 s12, s12, 0x3e0
	s_add_u32 s6, s23, s6
	s_addc_u32 s7, s24, s7
	v_cvt_pk_fp8_f32 v4, v12, v2 op_sel:[0,0,1]
	s_waitcnt lgkmcnt(0)
	v_med3_f32 v2, v10, -v13, v13
	v_med3_f32 v8, v11, -v13, v13
	s_add_u32 s6, s6, s2
	v_cvt_pk_fp8_f32 v5, v2, v8 op_sel:[0,0,1]
	s_addc_u32 s7, s7, 0
	v_or_b32_e32 v2, s12, v36
	v_lshl_add_u64 v[6:7], s[6:7], 0, v[0:1]
	v_lshlrev_b32_e32 v2, 10, v2
	v_lshl_add_u64 v[8:9], v[6:7], 0, v[2:3]
	ds_read2_b32 v[10:11], v37 offset0:8 offset1:41
	global_store_dwordx2 v[8:9], v[4:5], off
	ds_read2_b32 v[4:5], v37 offset0:74 offset1:107
	v_mov_b32_e32 v2, 0x43e00000
	ds_read2_b32 v[8:9], v37 offset0:140 offset1:173
	s_waitcnt lgkmcnt(2)
	v_med3_f32 v10, v10, -v2, v2
	v_med3_f32 v11, v11, -v2, v2
	s_waitcnt lgkmcnt(1)
	v_med3_f32 v12, v4, -v2, v2
	v_mov_b32_e32 v4, v3
	v_cvt_pk_fp8_f32 v4, v10, v11
	ds_read2_b32 v[10:11], v37 offset0:206 offset1:239
	v_mov_b32_e32 v13, 0x43e00000
	v_med3_f32 v2, v5, -v2, v2
	v_mov_b32_e32 v5, v3
	s_waitcnt lgkmcnt(1)
	v_med3_f32 v8, v8, -v13, v13
	v_med3_f32 v9, v9, -v13, v13
	v_cvt_pk_fp8_f32 v5, v8, v9
	v_cvt_pk_fp8_f32 v4, v12, v2 op_sel:[0,0,1]
	s_waitcnt lgkmcnt(0)
	v_med3_f32 v2, v10, -v13, v13
	v_med3_f32 v8, v11, -v13, v13
	v_cvt_pk_fp8_f32 v5, v2, v8 op_sel:[0,0,1]
	v_or_b32_e32 v2, s12, v38
	v_lshlrev_b32_e32 v2, 10, v2
	v_lshl_add_u64 v[8:9], v[6:7], 0, v[2:3]
	ds_read2_b32 v[10:11], v37 offset0:16 offset1:49
	global_store_dwordx2 v[8:9], v[4:5], off
	ds_read2_b32 v[4:5], v37 offset0:82 offset1:115
	v_mov_b32_e32 v2, 0x43e00000
	ds_read2_b32 v[8:9], v37 offset0:148 offset1:181
	s_waitcnt lgkmcnt(2)
	v_med3_f32 v10, v10, -v2, v2
	v_med3_f32 v11, v11, -v2, v2
	s_waitcnt lgkmcnt(1)
	v_med3_f32 v12, v4, -v2, v2
	v_mov_b32_e32 v4, v3
	v_cvt_pk_fp8_f32 v4, v10, v11
	ds_read2_b32 v[10:11], v37 offset0:214 offset1:247
	v_mov_b32_e32 v13, 0x43e00000
	v_med3_f32 v2, v5, -v2, v2
	v_mov_b32_e32 v5, v3
	s_waitcnt lgkmcnt(1)
	v_med3_f32 v8, v8, -v13, v13
	v_med3_f32 v9, v9, -v13, v13
	v_cvt_pk_fp8_f32 v5, v8, v9
	v_cvt_pk_fp8_f32 v4, v12, v2 op_sel:[0,0,1]
	s_waitcnt lgkmcnt(0)
	v_med3_f32 v2, v10, -v13, v13
	v_med3_f32 v8, v11, -v13, v13
	v_cvt_pk_fp8_f32 v5, v2, v8 op_sel:[0,0,1]
	v_or_b32_e32 v2, s12, v39
	v_lshlrev_b32_e32 v2, 10, v2
	v_lshl_add_u64 v[8:9], v[6:7], 0, v[2:3]
	ds_read2_b32 v[10:11], v37 offset0:24 offset1:57
	global_store_dwordx2 v[8:9], v[4:5], off
	ds_read2_b32 v[4:5], v37 offset0:90 offset1:123
	v_mov_b32_e32 v2, 0x43e00000
	ds_read2_b32 v[8:9], v37 offset0:156 offset1:189
	s_waitcnt lgkmcnt(2)
	v_med3_f32 v10, v10, -v2, v2
	v_med3_f32 v11, v11, -v2, v2
	s_waitcnt lgkmcnt(1)
	v_med3_f32 v12, v4, -v2, v2
	v_mov_b32_e32 v4, v3
	v_cvt_pk_fp8_f32 v4, v10, v11
	ds_read2_b32 v[10:11], v37 offset0:222 offset1:255
	v_mov_b32_e32 v13, 0x43e00000
	v_med3_f32 v2, v5, -v2, v2
	v_mov_b32_e32 v5, v3
	s_waitcnt lgkmcnt(1)
	v_med3_f32 v8, v8, -v13, v13
	v_med3_f32 v9, v9, -v13, v13
	v_cvt_pk_fp8_f32 v5, v8, v9
	v_cvt_pk_fp8_f32 v4, v12, v2 op_sel:[0,0,1]
	s_waitcnt lgkmcnt(0)
	v_med3_f32 v2, v10, -v13, v13
	v_med3_f32 v8, v11, -v13, v13
	v_cvt_pk_fp8_f32 v5, v2, v8 op_sel:[0,0,1]
	v_or_b32_e32 v2, s12, v40
	v_lshlrev_b32_e32 v2, 10, v2
	v_lshl_add_u64 v[6:7], v[6:7], 0, v[2:3]
	global_store_dwordx2 v[6:7], v[4:5], off
	s_waitcnt lgkmcnt(0)
